# GEMM unit boundaries: accumulators cleared with 64 v_mov_b64 literal-0 instead of 128 v_mov_b32 (on top of v098)
# speedup vs baseline: 1.0132x; 1.0132x over previous
.LBB0_425:
	s_lshl_b32 s35, s30, 19
	s_and_b64 s[6:7], s[0:1], exec
	s_cselect_b32 s39, s35, s42
	s_lshl_b32 s36, s34, 19
	s_and_b64 s[6:7], s[0:1], exec
	s_cselect_b32 s40, s36, s41
	s_add_i32 s41, s41, 0x60080
	s_addk_i32 s42, 0x100
	s_mov_b32 s43, -2
	v_mov_b64_e32 v[0:1], 0
	v_mov_b64_e32 v[2:3], 0
	v_mov_b64_e32 v[4:5], 0
	v_mov_b64_e32 v[6:7], 0
	v_mov_b64_e32 v[8:9], 0
	v_mov_b64_e32 v[10:11], 0
	v_mov_b64_e32 v[12:13], 0
	v_mov_b64_e32 v[14:15], 0
	v_mov_b64_e32 v[16:17], 0
	v_mov_b64_e32 v[18:19], 0
	v_mov_b64_e32 v[20:21], 0
	v_mov_b64_e32 v[22:23], 0
	v_mov_b64_e32 v[24:25], 0
	v_mov_b64_e32 v[26:27], 0
	v_mov_b64_e32 v[28:29], 0
	v_mov_b64_e32 v[30:31], 0
	v_mov_b64_e32 v[32:33], 0
	v_mov_b64_e32 v[34:35], 0
	v_mov_b64_e32 v[36:37], 0
	v_mov_b64_e32 v[38:39], 0
	v_mov_b64_e32 v[40:41], 0
	v_mov_b64_e32 v[42:43], 0
	v_mov_b64_e32 v[44:45], 0
	v_mov_b64_e32 v[46:47], 0
	v_mov_b64_e32 v[48:49], 0
	v_mov_b64_e32 v[50:51], 0
	v_mov_b64_e32 v[52:53], 0
	v_mov_b64_e32 v[54:55], 0
	v_mov_b64_e32 v[56:57], 0
	v_mov_b64_e32 v[58:59], 0
	v_mov_b64_e32 v[60:61], 0
	v_mov_b64_e32 v[62:63], 0
	v_mov_b64_e32 v[64:65], 0
	v_mov_b64_e32 v[66:67], 0
	v_mov_b64_e32 v[68:69], 0
	v_mov_b64_e32 v[70:71], 0
	v_mov_b64_e32 v[72:73], 0
	v_mov_b64_e32 v[74:75], 0
	v_mov_b64_e32 v[76:77], 0
	v_mov_b64_e32 v[78:79], 0
	v_mov_b64_e32 v[80:81], 0
	v_mov_b64_e32 v[82:83], 0
	v_mov_b64_e32 v[84:85], 0
	v_mov_b64_e32 v[86:87], 0
	v_mov_b64_e32 v[88:89], 0
	v_mov_b64_e32 v[90:91], 0
	v_mov_b64_e32 v[92:93], 0
	v_mov_b64_e32 v[94:95], 0
	v_mov_b64_e32 v[96:97], 0
	v_mov_b64_e32 v[98:99], 0
	v_mov_b64_e32 v[100:101], 0
	v_mov_b64_e32 v[102:103], 0
	v_mov_b64_e32 v[104:105], 0
	v_mov_b64_e32 v[106:107], 0
	v_mov_b64_e32 v[108:109], 0
	v_mov_b64_e32 v[110:111], 0
	v_mov_b64_e32 v[112:113], 0
	v_mov_b64_e32 v[114:115], 0
	v_mov_b64_e32 v[116:117], 0
	v_mov_b64_e32 v[118:119], 0
	v_mov_b64_e32 v[120:121], 0
	v_mov_b64_e32 v[122:123], 0
	v_mov_b64_e32 v[124:125], 0
	v_mov_b64_e32 v[126:127], 0

.LBB0_636:
	s_add_i32 s26, s16, 0x18000
	s_add_i32 s7, s21, 0x80
	s_mov_b32 m0, s26
	s_add_i32 s27, s16, 0x1a000
	s_waitcnt vmcnt(2)
	s_barrier
	buffer_load_dwordx4 v141, s[60:63], s7 offen lds
	s_add_i32 s7, s21, 0x8080
	s_mov_b32 m0, s27
	v_and_b32_e32 v1, 15, v0
	v_and_b32_e32 v2, 48, v0
	v_lshlrev_b32_e32 v0, 2, v0
	buffer_load_dwordx4 v141, s[60:63], s7 offen lds
	v_lshl_or_b32 v2, v1, 6, v2
	v_and_b32_e32 v3, 32, v0
	ds_read_b64 v[0:1], v140
	s_lshl_b32 s0, s0, 5
	s_lshl_b32 s25, s1, 6
	s_lshl_b32 s1, s1, 13
	s_and_b32 s0, s0, 0x60
	v_bitop3_b32 v4, v2, s1, v3 bitop3:0xde
	s_lshl_b32 s1, s0, 7
	s_add_i32 s28, s16, 0x8000
	v_bitop3_b32 v2, s1, v2, v3 bitop3:0xf6
	s_mov_b32 m0, s28
	s_movk_i32 s1, 0x80
	s_add_i32 s29, s16, 0xa000
	s_waitcnt lgkmcnt(0)
	buffer_load_dwordx4 v0, s[60:63], s1 offen lds
	s_mov_b32 m0, s29
	s_add_i32 s30, s16, 0x1c000
	buffer_load_dwordx4 v1, s[60:63], s1 offen lds
	s_add_i32 s1, s21, 0x10080
	s_mov_b32 m0, s30
	s_add_i32 s31, s16, 0x1e000
	buffer_load_dwordx4 v141, s[60:63], s1 offen lds
	s_add_i32 s1, s21, 0x18080
	s_mov_b32 m0, s31
	s_add_i32 s34, s16, 0xc000
	buffer_load_dwordx4 v141, s[60:63], s1 offen lds
	s_add_i32 s35, s16, 0xe000
	s_waitcnt vmcnt(6)
	s_cmpk_lt_u32 s6, 0x100
	v_or_b32_e32 v2, 0x10000, v2
	s_cselect_b64 s[6:7], -1, 0
	s_lshl_b32 s1, s59, 19
	s_or_b32 s36, s1, 0x1e00000
	s_or_b32 s37, s38, 0x1c00000
	s_bitset1_b32 s38, 25
	s_mov_b32 s39, 0
	v_add_u32_e32 v142, 0, v2
	v_add_u32_e32 v143, 0, v4
	s_lshl_b32 s64, s0, 1
	v_readlane_b32 s40, v251, 11
	v_readlane_b32 s41, v252, 18
	v_mov_b32_e32 v0, v134
	v_mov_b32_e32 v1, v134
	v_mov_b32_e32 v2, v134
	v_mov_b32_e32 v3, v134
	v_mov_b32_e32 v4, v134
	v_mov_b32_e32 v5, v134
	v_mov_b32_e32 v6, v134
	v_mov_b32_e32 v7, v134
	v_mov_b32_e32 v8, v134
	v_mov_b32_e32 v9, v134
	v_mov_b32_e32 v10, v134
	v_mov_b32_e32 v11, v134
	v_mov_b32_e32 v12, v134
	v_mov_b32_e32 v13, v134
	v_mov_b32_e32 v14, v134
	v_mov_b32_e32 v15, v134
	s_waitcnt vmcnt(19)
	v_mov_b32_e32 v16, v134
	v_mov_b32_e32 v17, v134
	v_mov_b32_e32 v18, v134
	v_mov_b32_e32 v19, v134
	s_waitcnt vmcnt(18)
	v_mov_b32_e32 v20, v134
	v_mov_b32_e32 v21, v134
	v_mov_b32_e32 v22, v134
	v_mov_b32_e32 v23, v134
	s_waitcnt vmcnt(17)
	v_mov_b32_e32 v24, v134
	v_mov_b32_e32 v25, v134
	v_mov_b32_e32 v26, v134
	v_mov_b32_e32 v27, v134
	s_waitcnt vmcnt(16)
	v_mov_b32_e32 v28, v134
	v_mov_b32_e32 v29, v134
	v_mov_b32_e32 v30, v134
	v_mov_b32_e32 v31, v134
	s_waitcnt vmcnt(15)
	v_mov_b32_e32 v32, v134
	v_mov_b32_e32 v33, v134
	v_mov_b32_e32 v34, v134
	v_mov_b32_e32 v35, v134
	v_mov_b32_e32 v36, v134
	v_mov_b32_e32 v37, v134
	v_mov_b32_e32 v38, v134
	v_mov_b32_e32 v39, v134
	v_mov_b32_e32 v40, v134
	v_mov_b32_e32 v41, v134
	v_mov_b32_e32 v42, v134
	v_mov_b32_e32 v43, v134
	v_mov_b32_e32 v44, v134
	v_mov_b32_e32 v45, v134
	v_mov_b32_e32 v46, v134
	v_mov_b32_e32 v47, v134
	v_mov_b32_e32 v48, v134
	v_mov_b32_e32 v49, v134
	v_mov_b32_e32 v50, v134
	v_mov_b32_e32 v51, v134
	v_mov_b32_e32 v52, v134
	v_mov_b32_e32 v53, v134
	v_mov_b32_e32 v54, v134
	v_mov_b32_e32 v55, v134
	s_waitcnt vmcnt(14)
	v_mov_b64_e32 v[56:57], 0
	v_mov_b64_e32 v[58:59], 0
	v_mov_b64_e32 v[60:61], 0
	v_mov_b64_e32 v[62:63], 0
	v_mov_b64_e32 v[64:65], 0
	v_mov_b64_e32 v[66:67], 0
	v_mov_b64_e32 v[68:69], 0
	v_mov_b64_e32 v[70:71], 0
	v_mov_b64_e32 v[72:73], 0
	v_mov_b64_e32 v[74:75], 0
	v_mov_b64_e32 v[76:77], 0
	v_mov_b64_e32 v[78:79], 0
	v_mov_b64_e32 v[80:81], 0
	v_mov_b64_e32 v[82:83], 0
	v_mov_b64_e32 v[84:85], 0
	v_mov_b64_e32 v[86:87], 0
	v_mov_b64_e32 v[88:89], 0
	v_mov_b64_e32 v[90:91], 0
	v_mov_b64_e32 v[92:93], 0
	v_mov_b64_e32 v[94:95], 0
	v_mov_b64_e32 v[96:97], 0
	v_mov_b64_e32 v[98:99], 0
	v_mov_b64_e32 v[100:101], 0
	v_mov_b64_e32 v[102:103], 0
	v_mov_b64_e32 v[104:105], 0
	v_mov_b64_e32 v[106:107], 0
	v_mov_b64_e32 v[108:109], 0
	v_mov_b64_e32 v[110:111], 0
	v_mov_b64_e32 v[112:113], 0
	v_mov_b64_e32 v[114:115], 0
	v_mov_b64_e32 v[116:117], 0
	v_mov_b64_e32 v[118:119], 0
	v_mov_b64_e32 v[120:121], 0
	v_mov_b64_e32 v[122:123], 0
	v_mov_b64_e32 v[124:125], 0
	v_mov_b64_e32 v[126:127], 0
	s_barrier
	s_branch .LBB0_639
.LBB0_637:
	s_mov_b32 s40, s46
	s_mov_b32 s41, s42
	s_mov_b32 s43, s47
	s_mov_b32 s44, s45
	s_mov_b32 s21, s49
	s_mov_b32 s39, s48
	v_mov_b64_e32 v[0:1], 0
	v_mov_b64_e32 v[2:3], 0
	v_mov_b64_e32 v[4:5], 0
	v_mov_b64_e32 v[6:7], 0
	v_mov_b64_e32 v[8:9], 0
	v_mov_b64_e32 v[10:11], 0
	v_mov_b64_e32 v[12:13], 0
	v_mov_b64_e32 v[14:15], 0
	v_mov_b64_e32 v[16:17], 0
	v_mov_b64_e32 v[18:19], 0
	v_mov_b64_e32 v[20:21], 0
	v_mov_b64_e32 v[22:23], 0
	v_mov_b64_e32 v[24:25], 0
	v_mov_b64_e32 v[26:27], 0
	v_mov_b64_e32 v[28:29], 0
	v_mov_b64_e32 v[30:31], 0
	v_mov_b64_e32 v[32:33], 0
	v_mov_b64_e32 v[34:35], 0
	v_mov_b64_e32 v[36:37], 0
	v_mov_b64_e32 v[38:39], 0
	v_mov_b64_e32 v[40:41], 0
	v_mov_b64_e32 v[42:43], 0
	v_mov_b64_e32 v[44:45], 0
	v_mov_b64_e32 v[46:47], 0
	v_mov_b64_e32 v[48:49], 0
	v_mov_b64_e32 v[50:51], 0
	v_mov_b64_e32 v[52:53], 0
	v_mov_b64_e32 v[54:55], 0
	v_mov_b64_e32 v[56:57], 0
	v_mov_b64_e32 v[58:59], 0
	v_mov_b64_e32 v[60:61], 0
	v_mov_b64_e32 v[62:63], 0
	v_mov_b64_e32 v[64:65], 0
	v_mov_b64_e32 v[66:67], 0
	v_mov_b64_e32 v[68:69], 0
	v_mov_b64_e32 v[70:71], 0
	v_mov_b64_e32 v[72:73], 0
	v_mov_b64_e32 v[74:75], 0
	v_mov_b64_e32 v[76:77], 0
	v_mov_b64_e32 v[78:79], 0
	v_mov_b64_e32 v[80:81], 0
	v_mov_b64_e32 v[82:83], 0
	v_mov_b64_e32 v[84:85], 0
	v_mov_b64_e32 v[86:87], 0
	v_mov_b64_e32 v[88:89], 0
	v_mov_b64_e32 v[90:91], 0
	v_mov_b64_e32 v[92:93], 0
	v_mov_b64_e32 v[94:95], 0
	v_mov_b64_e32 v[96:97], 0
	v_mov_b64_e32 v[98:99], 0
	v_mov_b64_e32 v[100:101], 0
	v_mov_b64_e32 v[102:103], 0
	v_mov_b64_e32 v[104:105], 0
	v_mov_b64_e32 v[106:107], 0
	v_mov_b64_e32 v[108:109], 0
	v_mov_b64_e32 v[110:111], 0
	v_mov_b64_e32 v[112:113], 0
	v_mov_b64_e32 v[114:115], 0
	v_mov_b64_e32 v[116:117], 0
	v_mov_b64_e32 v[118:119], 0
	v_mov_b64_e32 v[120:121], 0
	v_mov_b64_e32 v[122:123], 0
	v_mov_b64_e32 v[124:125], 0
	v_mov_b64_e32 v[126:127], 0

.LBB0_1160:
	s_lshl_b32 s52, s49, 19
	s_and_b64 s[10:11], s[0:1], exec
	s_cselect_b32 s56, s52, s59
	s_lshl_b32 s53, s51, 19
	s_and_b64 s[10:11], s[0:1], exec
	s_cselect_b32 s57, s53, s58
	s_add_i32 s58, s58, 0x60080
	s_addk_i32 s59, 0x100
	s_mov_b32 s60, -2
	v_mov_b32_e32 v0, v150
	v_mov_b32_e32 v1, v150
	v_mov_b32_e32 v2, v150
	v_mov_b32_e32 v3, v150
	v_mov_b32_e32 v4, v150
	v_mov_b32_e32 v5, v150
	v_mov_b32_e32 v6, v150
	v_mov_b32_e32 v7, v150
	s_waitcnt vmcnt(14)
	v_mov_b64_e32 v[8:9], 0
	v_mov_b64_e32 v[10:11], 0
	v_mov_b64_e32 v[12:13], 0
	v_mov_b64_e32 v[14:15], 0
	v_mov_b64_e32 v[16:17], 0
	v_mov_b64_e32 v[18:19], 0
	v_mov_b64_e32 v[20:21], 0
	v_mov_b64_e32 v[22:23], 0
	v_mov_b64_e32 v[24:25], 0
	v_mov_b64_e32 v[26:27], 0
	v_mov_b64_e32 v[28:29], 0
	v_mov_b64_e32 v[30:31], 0
	v_mov_b64_e32 v[32:33], 0
	v_mov_b64_e32 v[34:35], 0
	v_mov_b64_e32 v[36:37], 0
	v_mov_b64_e32 v[38:39], 0
	v_mov_b64_e32 v[40:41], 0
	v_mov_b64_e32 v[42:43], 0
	v_mov_b64_e32 v[44:45], 0
	v_mov_b64_e32 v[46:47], 0
	v_mov_b64_e32 v[48:49], 0
	v_mov_b64_e32 v[50:51], 0
	v_mov_b64_e32 v[52:53], 0
	v_mov_b64_e32 v[54:55], 0
	v_mov_b64_e32 v[56:57], 0
	v_mov_b64_e32 v[58:59], 0
	v_mov_b64_e32 v[60:61], 0
	v_mov_b64_e32 v[62:63], 0
	v_mov_b64_e32 v[64:65], 0
	v_mov_b64_e32 v[66:67], 0
	v_mov_b64_e32 v[68:69], 0
	v_mov_b64_e32 v[70:71], 0
	v_mov_b64_e32 v[72:73], 0
	v_mov_b64_e32 v[74:75], 0
	v_mov_b64_e32 v[76:77], 0
	v_mov_b64_e32 v[78:79], 0
	v_mov_b64_e32 v[80:81], 0
	v_mov_b64_e32 v[82:83], 0
	v_mov_b64_e32 v[84:85], 0
	v_mov_b64_e32 v[86:87], 0
	v_mov_b64_e32 v[88:89], 0
	v_mov_b64_e32 v[90:91], 0
	v_mov_b64_e32 v[92:93], 0
	v_mov_b64_e32 v[94:95], 0
	v_mov_b64_e32 v[96:97], 0
	v_mov_b64_e32 v[98:99], 0
	v_mov_b64_e32 v[100:101], 0
	v_mov_b64_e32 v[102:103], 0
	v_mov_b64_e32 v[104:105], 0
	v_mov_b64_e32 v[106:107], 0
	v_mov_b64_e32 v[108:109], 0
	v_mov_b64_e32 v[110:111], 0
	v_mov_b64_e32 v[112:113], 0
	v_mov_b64_e32 v[114:115], 0
	v_mov_b64_e32 v[116:117], 0
	v_mov_b64_e32 v[118:119], 0
	v_mov_b64_e32 v[120:121], 0
	v_mov_b64_e32 v[122:123], 0
	v_mov_b64_e32 v[124:125], 0
	v_mov_b64_e32 v[126:127], 0

.LBB0_1182:
	s_lshl_b32 s74, s64, 19
	s_and_b64 s[2:3], s[0:1], exec
	s_cselect_b32 s2, s74, s10
	s_lshl_b32 s75, s73, 19
	s_and_b64 s[30:31], s[0:1], exec
	s_cselect_b32 s3, s75, s11
	s_add_i32 s30, s11, 0x60080
	s_add_i32 s31, s10, 0x100
	s_mov_b32 s34, -2
	v_mov_b32_e32 v0, v245
	v_mov_b32_e32 v1, v245
	v_mov_b32_e32 v2, v245
	v_mov_b32_e32 v3, v245
	v_mov_b32_e32 v4, v245
	v_mov_b32_e32 v5, v245
	v_mov_b32_e32 v6, v245
	v_mov_b32_e32 v7, v245
	s_waitcnt vmcnt(0)
	v_mov_b64_e32 v[8:9], 0
	v_mov_b64_e32 v[10:11], 0
	v_mov_b64_e32 v[12:13], 0
	v_mov_b64_e32 v[14:15], 0
	v_mov_b64_e32 v[16:17], 0
	v_mov_b64_e32 v[18:19], 0
	v_mov_b64_e32 v[20:21], 0
	v_mov_b64_e32 v[22:23], 0
	v_mov_b64_e32 v[24:25], 0
	v_mov_b64_e32 v[26:27], 0
	v_mov_b64_e32 v[28:29], 0
	v_mov_b64_e32 v[30:31], 0
	v_mov_b64_e32 v[32:33], 0
	v_mov_b64_e32 v[34:35], 0
	v_mov_b64_e32 v[36:37], 0
	v_mov_b64_e32 v[38:39], 0
	v_mov_b64_e32 v[40:41], 0
	v_mov_b64_e32 v[42:43], 0
	v_mov_b64_e32 v[44:45], 0
	v_mov_b64_e32 v[46:47], 0
	v_mov_b64_e32 v[48:49], 0
	v_mov_b64_e32 v[50:51], 0
	v_mov_b64_e32 v[52:53], 0
	v_mov_b64_e32 v[54:55], 0
	v_mov_b64_e32 v[56:57], 0
	v_mov_b64_e32 v[58:59], 0
	v_mov_b64_e32 v[60:61], 0
	v_mov_b64_e32 v[62:63], 0
	v_mov_b64_e32 v[64:65], 0
	v_mov_b64_e32 v[66:67], 0
	v_mov_b64_e32 v[68:69], 0
	v_mov_b64_e32 v[70:71], 0
	v_mov_b64_e32 v[72:73], 0
	v_mov_b64_e32 v[74:75], 0
	v_mov_b64_e32 v[76:77], 0
	v_mov_b64_e32 v[78:79], 0
	v_mov_b64_e32 v[80:81], 0
	v_mov_b64_e32 v[82:83], 0
	v_mov_b64_e32 v[84:85], 0
	v_mov_b64_e32 v[86:87], 0
	v_mov_b64_e32 v[88:89], 0
	v_mov_b64_e32 v[90:91], 0
	v_mov_b64_e32 v[92:93], 0
	v_mov_b64_e32 v[94:95], 0
	v_mov_b64_e32 v[96:97], 0
	v_mov_b64_e32 v[98:99], 0
	v_mov_b64_e32 v[100:101], 0
	v_mov_b64_e32 v[102:103], 0
	v_mov_b64_e32 v[104:105], 0
	v_mov_b64_e32 v[106:107], 0
	v_mov_b64_e32 v[108:109], 0
	v_mov_b64_e32 v[110:111], 0
	v_mov_b64_e32 v[112:113], 0
	v_mov_b64_e32 v[114:115], 0
	v_mov_b64_e32 v[116:117], 0
	v_mov_b64_e32 v[118:119], 0
	v_mov_b64_e32 v[120:121], 0
	v_mov_b64_e32 v[122:123], 0
	v_mov_b64_e32 v[124:125], 0
	v_mov_b64_e32 v[126:127], 0

.LBB0_1412:
	s_add_u32 s8, s18, 0x1fc00000
	s_addc_u32 s6, s19, 0
	s_add_u32 s12, s18, 0x1b400000
	v_and_b32_e32 v1, 15, v196
	v_and_b32_e32 v2, 48, v196
	s_addc_u32 s7, s19, 0
	s_lshl_b32 s9, s4, 6
	v_lshl_or_b32 v1, v1, 6, v2
	v_lshlrev_b32_e32 v2, 2, v196
	s_and_b32 s5, s5, 3
	v_writelane_b32 v253, s9, 61
	s_lshl_b32 s9, s4, 13
	v_and_b32_e32 v2, 32, v2
	v_bitop3_b32 v3, v1, s9, v2 bitop3:0xde
	s_lshl_b32 s9, s5, 5
	v_writelane_b32 v253, s9, 63
	s_lshl_b32 s9, s5, 12
	s_add_i32 s83, s73, 0x18000
	v_bitop3_b32 v1, s9, v1, v2 bitop3:0xf6
	s_add_i32 s9, s66, 0x80
	s_mov_b32 m0, s83
	s_add_i32 s84, s73, 0x1a000
	s_waitcnt vmcnt(2)
	s_barrier
	buffer_load_dwordx4 v194, s[60:63], s9 offen lds
	s_add_i32 s9, s9, s2
	s_mov_b32 m0, s84
	s_add_i32 s85, s73, 0x8000
	buffer_load_dwordx4 v194, s[60:63], s9 offen lds
	s_add_i32 s9, s57, 0x80
	s_mov_b32 m0, s85
	s_add_i32 s86, s73, 0xa000
	buffer_load_dwordx4 v192, s[60:63], s9 offen lds
	s_add_i32 s9, s9, s2
	s_mov_b32 m0, s86
	s_add_i32 s87, s73, 0x1c000
	buffer_load_dwordx4 v192, s[60:63], s9 offen lds
	s_addk_i32 s3, 0x80
	s_mov_b32 m0, s87
	s_add_i32 s90, s73, 0x1e000
	buffer_load_dwordx4 v194, s[60:63], s3 offen lds
	s_add_i32 s3, s3, s2
	s_mov_b32 m0, s90
	s_cmp_lt_u32 s10, 64
	buffer_load_dwordx4 v194, s[60:63], s3 offen lds
	s_cselect_b64 s[24:25], -1, 0
	s_add_i32 s91, s73, 0xc000
	s_add_i32 s92, s73, 0xe000
	s_cmpk_lt_u32 s10, 0x100
	s_cselect_b64 s[26:27], -1, 0
	s_and_b32 s13, s7, 0xffff
	s_lshl_b32 s5, s5, 6
	s_lshl_b32 s94, s4, 17
	s_and_b32 s9, s6, 0xffff
	s_cmp_lt_i32 s95, s1
	v_writelane_b32 v253, s5, 56
	s_cselect_b64 s[4:5], -1, 0
	v_cmp_eq_u32_e64 s[2:3], 0, v0
	v_cndmask_b32_e64 v0, 0, 1, s[4:5]
	s_cmp_lt_i32 s95, s0
	v_readfirstlane_b32 s4, v0
	s_waitcnt vmcnt(6)
	v_or_b32_e32 v1, 0x10000, v1
	s_mov_b32 s10, -1
	v_writelane_b32 v254, s4, 5
	s_cselect_b32 s4, 0, 3
	s_sub_i32 s5, s93, s0
	s_sub_i32 s0, s95, s0
	v_writelane_b32 v254, s4, 7
	s_mul_i32 s4, s51, s93
	s_add_i32 s0, s0, s1
	v_writelane_b32 v254, s5, 11
	s_add_i32 s0, s0, s4
	v_writelane_b32 v254, s0, 13
	s_add_i32 s0, s4, s95
	s_mov_b32 s36, 0
	s_mov_b32 s11, s63
	v_writelane_b32 v254, s0, 9
	v_add_u32_e32 v199, 0, v1
	v_add_u32_e32 v200, 0, v3
	s_mov_b32 s64, s10
	v_mov_b64_e32 v[64:65], 0
	v_mov_b64_e32 v[66:67], 0
	v_mov_b64_e32 v[68:69], 0
	v_mov_b64_e32 v[70:71], 0
	v_mov_b64_e32 v[72:73], 0
	v_mov_b64_e32 v[74:75], 0
	v_mov_b64_e32 v[76:77], 0
	v_mov_b64_e32 v[78:79], 0
	v_mov_b64_e32 v[80:81], 0
	v_mov_b64_e32 v[82:83], 0
	v_mov_b64_e32 v[84:85], 0
	v_mov_b64_e32 v[86:87], 0
	v_mov_b64_e32 v[88:89], 0
	v_mov_b64_e32 v[90:91], 0
	v_mov_b64_e32 v[92:93], 0
	v_mov_b64_e32 v[94:95], 0
	v_mov_b64_e32 v[96:97], 0
	v_mov_b64_e32 v[98:99], 0
	v_mov_b64_e32 v[100:101], 0
	v_mov_b64_e32 v[102:103], 0
	v_mov_b64_e32 v[104:105], 0
	v_mov_b64_e32 v[106:107], 0
	v_mov_b64_e32 v[108:109], 0
	v_mov_b64_e32 v[110:111], 0
	v_mov_b64_e32 v[112:113], 0
	v_mov_b64_e32 v[114:115], 0
	v_mov_b64_e32 v[116:117], 0
	v_mov_b64_e32 v[118:119], 0
	v_mov_b64_e32 v[120:121], 0
	v_mov_b64_e32 v[122:123], 0
	v_mov_b64_e32 v[124:125], 0
	v_mov_b64_e32 v[126:127], 0
	v_mov_b64_e32 v[128:129], 0
	v_mov_b64_e32 v[130:131], 0
	v_mov_b64_e32 v[132:133], 0
	v_mov_b64_e32 v[134:135], 0
	v_mov_b64_e32 v[136:137], 0
	v_mov_b64_e32 v[138:139], 0
	v_mov_b64_e32 v[140:141], 0
	v_mov_b64_e32 v[142:143], 0
	v_mov_b64_e32 v[144:145], 0
	v_mov_b64_e32 v[146:147], 0
	v_mov_b64_e32 v[148:149], 0
	v_mov_b64_e32 v[150:151], 0
	v_mov_b64_e32 v[152:153], 0
	v_mov_b64_e32 v[154:155], 0
	v_mov_b64_e32 v[156:157], 0
	v_mov_b64_e32 v[158:159], 0
	v_mov_b64_e32 v[160:161], 0
	v_mov_b64_e32 v[162:163], 0
	v_mov_b64_e32 v[164:165], 0
	v_mov_b64_e32 v[166:167], 0
	v_mov_b64_e32 v[168:169], 0
	v_mov_b64_e32 v[170:171], 0
	v_mov_b64_e32 v[172:173], 0
	v_mov_b64_e32 v[174:175], 0
	v_mov_b64_e32 v[176:177], 0
	v_mov_b64_e32 v[178:179], 0
	v_mov_b64_e32 v[180:181], 0
	v_mov_b64_e32 v[182:183], 0
	v_mov_b64_e32 v[184:185], 0
	v_mov_b64_e32 v[186:187], 0
	v_mov_b64_e32 v[188:189], 0
	v_mov_b64_e32 v[190:191], 0
	s_barrier
	s_branch .LBB0_1415
.LBB0_1413:
	s_mov_b32 s52, s37
	s_mov_b32 s53, s1
	s_mov_b32 s97, s54
	s_mov_b32 s55, s48
	s_mov_b32 s66, s67
	s_mov_b32 s57, s56
	s_mov_b32 s72, s46
	s_mov_b32 s36, s95
	v_mov_b64_e32 v[64:65], 0
	v_mov_b64_e32 v[66:67], 0
	v_mov_b64_e32 v[68:69], 0
	v_mov_b64_e32 v[70:71], 0
	v_mov_b64_e32 v[72:73], 0
	v_mov_b64_e32 v[74:75], 0
	v_mov_b64_e32 v[76:77], 0
	v_mov_b64_e32 v[78:79], 0
	v_mov_b64_e32 v[80:81], 0
	v_mov_b64_e32 v[82:83], 0
	v_mov_b64_e32 v[84:85], 0
	v_mov_b64_e32 v[86:87], 0
	v_mov_b64_e32 v[88:89], 0
	v_mov_b64_e32 v[90:91], 0
	v_mov_b64_e32 v[92:93], 0
	v_mov_b64_e32 v[94:95], 0
	v_mov_b64_e32 v[96:97], 0
	v_mov_b64_e32 v[98:99], 0
	v_mov_b64_e32 v[100:101], 0
	v_mov_b64_e32 v[102:103], 0
	v_mov_b64_e32 v[104:105], 0
	v_mov_b64_e32 v[106:107], 0
	v_mov_b64_e32 v[108:109], 0
	v_mov_b64_e32 v[110:111], 0
	v_mov_b64_e32 v[112:113], 0
	v_mov_b64_e32 v[114:115], 0
	v_mov_b64_e32 v[116:117], 0
	v_mov_b64_e32 v[118:119], 0
	v_mov_b64_e32 v[120:121], 0
	v_mov_b64_e32 v[122:123], 0
	v_mov_b64_e32 v[124:125], 0
	v_mov_b64_e32 v[126:127], 0
	v_mov_b64_e32 v[128:129], 0
	v_mov_b64_e32 v[130:131], 0
	v_mov_b64_e32 v[132:133], 0
	v_mov_b64_e32 v[134:135], 0
	v_mov_b64_e32 v[136:137], 0
	v_mov_b64_e32 v[138:139], 0
	v_mov_b64_e32 v[140:141], 0
	v_mov_b64_e32 v[142:143], 0
	v_mov_b64_e32 v[144:145], 0
	v_mov_b64_e32 v[146:147], 0
	v_mov_b64_e32 v[148:149], 0
	v_mov_b64_e32 v[150:151], 0
	v_mov_b64_e32 v[152:153], 0
	v_mov_b64_e32 v[154:155], 0
	v_mov_b64_e32 v[156:157], 0
	v_mov_b64_e32 v[158:159], 0
	v_mov_b64_e32 v[160:161], 0
	v_mov_b64_e32 v[162:163], 0
	v_mov_b64_e32 v[164:165], 0
	v_mov_b64_e32 v[166:167], 0
	v_mov_b64_e32 v[168:169], 0
	v_mov_b64_e32 v[170:171], 0
	v_mov_b64_e32 v[172:173], 0
	v_mov_b64_e32 v[174:175], 0
	v_mov_b64_e32 v[176:177], 0
	v_mov_b64_e32 v[178:179], 0
	v_mov_b64_e32 v[180:181], 0
	v_mov_b64_e32 v[182:183], 0
	v_mov_b64_e32 v[184:185], 0
	v_mov_b64_e32 v[186:187], 0
	v_mov_b64_e32 v[188:189], 0
	v_mov_b64_e32 v[190:191], 0

.LBB0_1569:
	s_lshl_b32 s38, s35, 19
	s_and_b64 s[6:7], s[0:1], exec
	s_cselect_b32 s40, s38, s43
	s_lshl_b32 s39, s37, 19
	s_and_b64 s[6:7], s[0:1], exec
	s_cselect_b32 s41, s39, s42
	s_add_i32 s42, s42, 0x60080
	s_addk_i32 s43, 0x100
	s_mov_b32 s44, -2
	v_mov_b64_e32 v[0:1], 0
	v_mov_b64_e32 v[2:3], 0
	v_mov_b64_e32 v[4:5], 0
	v_mov_b64_e32 v[6:7], 0
	v_mov_b64_e32 v[8:9], 0
	v_mov_b64_e32 v[10:11], 0
	v_mov_b64_e32 v[12:13], 0
	v_mov_b64_e32 v[14:15], 0
	v_mov_b64_e32 v[16:17], 0
	v_mov_b64_e32 v[18:19], 0
	v_mov_b64_e32 v[20:21], 0
	v_mov_b64_e32 v[22:23], 0
	v_mov_b64_e32 v[24:25], 0
	v_mov_b64_e32 v[26:27], 0
	v_mov_b64_e32 v[28:29], 0
	v_mov_b64_e32 v[30:31], 0
	v_mov_b64_e32 v[32:33], 0
	v_mov_b64_e32 v[34:35], 0
	v_mov_b64_e32 v[36:37], 0
	v_mov_b64_e32 v[38:39], 0
	v_mov_b64_e32 v[40:41], 0
	v_mov_b64_e32 v[42:43], 0
	v_mov_b64_e32 v[44:45], 0
	v_mov_b64_e32 v[46:47], 0
	v_mov_b64_e32 v[48:49], 0
	v_mov_b64_e32 v[50:51], 0
	v_mov_b64_e32 v[52:53], 0
	v_mov_b64_e32 v[54:55], 0
	v_mov_b64_e32 v[56:57], 0
	v_mov_b64_e32 v[58:59], 0
	v_mov_b64_e32 v[60:61], 0
	v_mov_b64_e32 v[62:63], 0
	v_mov_b64_e32 v[64:65], 0
	v_mov_b64_e32 v[66:67], 0
	v_mov_b64_e32 v[68:69], 0
	v_mov_b64_e32 v[70:71], 0
	v_mov_b64_e32 v[72:73], 0
	v_mov_b64_e32 v[74:75], 0
	v_mov_b64_e32 v[76:77], 0
	v_mov_b64_e32 v[78:79], 0
	v_mov_b64_e32 v[80:81], 0
	v_mov_b64_e32 v[82:83], 0
	v_mov_b64_e32 v[84:85], 0
	v_mov_b64_e32 v[86:87], 0
	v_mov_b64_e32 v[88:89], 0
	v_mov_b64_e32 v[90:91], 0
	v_mov_b64_e32 v[92:93], 0
	v_mov_b64_e32 v[94:95], 0
	v_mov_b64_e32 v[96:97], 0
	v_mov_b64_e32 v[98:99], 0
	v_mov_b64_e32 v[100:101], 0
	v_mov_b64_e32 v[102:103], 0
	v_mov_b64_e32 v[104:105], 0
	v_mov_b64_e32 v[106:107], 0
	v_mov_b64_e32 v[108:109], 0
	v_mov_b64_e32 v[110:111], 0
	v_mov_b64_e32 v[112:113], 0
	v_mov_b64_e32 v[114:115], 0
	v_mov_b64_e32 v[116:117], 0
	v_mov_b64_e32 v[118:119], 0
	v_mov_b64_e32 v[120:121], 0
	v_mov_b64_e32 v[122:123], 0
	v_mov_b64_e32 v[124:125], 0
	v_mov_b64_e32 v[126:127], 0

.LBB0_1645:
	s_mul_i32 s77, s64, 0xb0000
	s_and_b64 s[2:3], s[0:1], exec
	s_mul_i32 s78, s76, 0xb0000
	s_cselect_b32 s2, s77, s10
	s_cselect_b32 s3, s78, s11
	s_add_i32 s12, s11, 0x84080
	s_add_i32 s13, s10, 0x100
	s_mov_b32 s14, -2
	v_mov_b64_e32 v[0:1], 0
	v_mov_b64_e32 v[2:3], 0
	v_mov_b64_e32 v[4:5], 0
	v_mov_b64_e32 v[6:7], 0
	v_mov_b64_e32 v[8:9], 0
	v_mov_b64_e32 v[10:11], 0
	v_mov_b64_e32 v[12:13], 0
	v_mov_b64_e32 v[14:15], 0
	v_mov_b64_e32 v[16:17], 0
	v_mov_b64_e32 v[18:19], 0
	v_mov_b64_e32 v[20:21], 0
	v_mov_b64_e32 v[22:23], 0
	v_mov_b64_e32 v[24:25], 0
	v_mov_b64_e32 v[26:27], 0
	v_mov_b64_e32 v[28:29], 0
	v_mov_b64_e32 v[30:31], 0
	v_mov_b64_e32 v[32:33], 0
	v_mov_b64_e32 v[34:35], 0
	v_mov_b64_e32 v[36:37], 0
	v_mov_b64_e32 v[38:39], 0
	v_mov_b64_e32 v[40:41], 0
	v_mov_b64_e32 v[42:43], 0
	v_mov_b64_e32 v[44:45], 0
	v_mov_b64_e32 v[46:47], 0
	v_mov_b64_e32 v[48:49], 0
	v_mov_b64_e32 v[50:51], 0
	v_mov_b64_e32 v[52:53], 0
	v_mov_b64_e32 v[54:55], 0
	v_mov_b64_e32 v[56:57], 0
	v_mov_b64_e32 v[58:59], 0
	v_mov_b64_e32 v[60:61], 0
	v_mov_b64_e32 v[62:63], 0
	v_mov_b64_e32 v[64:65], 0
	v_mov_b64_e32 v[66:67], 0
	v_mov_b64_e32 v[68:69], 0
	v_mov_b64_e32 v[70:71], 0
	v_mov_b64_e32 v[72:73], 0
	v_mov_b64_e32 v[74:75], 0
	v_mov_b64_e32 v[76:77], 0
	v_mov_b64_e32 v[78:79], 0
	v_mov_b64_e32 v[80:81], 0
	v_mov_b64_e32 v[82:83], 0
	v_mov_b64_e32 v[84:85], 0
	v_mov_b64_e32 v[86:87], 0
	v_mov_b64_e32 v[88:89], 0
	v_mov_b64_e32 v[90:91], 0
	v_mov_b64_e32 v[92:93], 0
	v_mov_b64_e32 v[94:95], 0
	v_mov_b64_e32 v[96:97], 0
	v_mov_b64_e32 v[98:99], 0
	v_mov_b64_e32 v[100:101], 0
	v_mov_b64_e32 v[102:103], 0
	v_mov_b64_e32 v[104:105], 0
	v_mov_b64_e32 v[106:107], 0
	v_mov_b64_e32 v[108:109], 0
	v_mov_b64_e32 v[110:111], 0
	v_mov_b64_e32 v[112:113], 0
	v_mov_b64_e32 v[114:115], 0
	v_mov_b64_e32 v[116:117], 0
	v_mov_b64_e32 v[118:119], 0
	v_mov_b64_e32 v[120:121], 0
	v_mov_b64_e32 v[122:123], 0
	v_mov_b64_e32 v[124:125], 0
	v_mov_b64_e32 v[126:127], 0
